# speedup vs baseline: 1.0018x; 1.0004x over previous
_Z11proj_kernelPKcPKfS2_Pf:
	s_load_dwordx8 s[4:11], s[0:1], 0x0
	s_lshl_b32 s0, s2, 6
	s_and_b32 s0, s0, 0x1c0
	s_ashr_i32 s2, s2, 3
	s_add_i32 s0, s0, s2
	s_ashr_i32 s0, s0, 5
	s_and_b32 s26, s2, 3
	s_ashr_i32 s1, s0, 31
	s_lshl_b32 s2, s2, 5
	s_lshl_b32 s12, s26, 16
	s_and_b32 s27, s2, 0x380
	s_lshl_b64 s[2:3], s[0:1], 18
	s_waitcnt lgkmcnt(0)
	s_add_u32 s1, s4, s2
	s_addc_u32 s13, s5, s3
	s_add_u32 s2, s4, s12
	v_lshrrev_b32_e32 v1, 4, v0
	s_addc_u32 s3, s5, 0
	s_lshl_b32 s4, s27, 8
	v_xor_b32_e32 v4, v1, v0
	s_add_u32 s4, s1, s4
	v_lshlrev_b32_e32 v130, 9, v1
	v_lshlrev_b32_e32 v1, 4, v4
	s_addc_u32 s5, s13, 0
	v_mov_b32_e32 v131, 0
	v_and_b32_e32 v4, 0xf0, v1
	v_lshrrev_b32_e32 v1, 1, v0
	v_mov_b32_e32 v5, v131
	v_lshrrev_b32_e32 v192, 1, v130
	v_mov_b32_e32 v193, 0
	v_lshl_add_u64 v[6:7], s[4:5], 0, v[192:193]
	v_and_b32_e32 v136, 64, v1
	v_lshlrev_b32_e32 v1, 4, v0
	v_lshl_add_u64 v[2:3], s[2:3], 0, v[130:131]
	v_lshl_add_u64 v[134:135], v[6:7], 0, v[4:5]
	v_add_u32_e32 v6, 0, v1
	v_lshl_add_u64 v[132:133], v[2:3], 0, v[4:5]
	s_mov_b64 s[2:3], 0x280000
	v_readfirstlane_b32 s5, v6
	v_lshl_add_u64 v[2:3], v[132:133], 0, s[2:3]
	s_mov_b32 m0, s5
	s_mov_b64 s[2:3], 0x4900000
	global_load_lds_dwordx4 v[2:3], off
	v_add_u32_e32 v2, 0x8000, v6
	v_lshl_add_u64 v[4:5], v[134:135], 0, s[2:3]
	v_readfirstlane_b32 s4, v2
	s_mov_b32 m0, s4
	s_mov_b64 s[2:3], 0x282000
	global_load_lds_dwordx4 v[4:5], off
	v_add_u32_e32 v4, 0x1000, v6
	v_lshl_add_u64 v[2:3], v[132:133], 0, s[2:3]
	v_readfirstlane_b32 s12, v4
	v_add_u32_e32 v4, 0x9000, v6
	s_mov_b32 m0, s12
	s_mov_b64 s[2:3], 0x4901000
	v_readfirstlane_b32 s13, v4
	v_add_u32_e32 v4, 0x2000, v6
	global_load_lds_dwordx4 v[2:3], off
	v_lshl_add_u64 v[2:3], v[134:135], 0, s[2:3]
	s_mov_b32 m0, s13
	s_mov_b64 s[2:3], 0x284000
	v_readfirstlane_b32 s14, v4
	v_add_u32_e32 v4, 0xa000, v6
	global_load_lds_dwordx4 v[2:3], off
	v_lshl_add_u64 v[2:3], v[132:133], 0, s[2:3]
	s_mov_b32 m0, s14
	s_mov_b64 s[2:3], 0x4902000
	v_readfirstlane_b32 s15, v4
	v_add_u32_e32 v4, 0x3000, v6
	global_load_lds_dwordx4 v[2:3], off
	v_lshl_add_u64 v[2:3], v[134:135], 0, s[2:3]
	s_mov_b32 m0, s15
	s_mov_b64 s[2:3], 0x286000
	v_readfirstlane_b32 s16, v4
	v_add_u32_e32 v4, 0xb000, v6
	global_load_lds_dwordx4 v[2:3], off
	v_lshl_add_u64 v[2:3], v[132:133], 0, s[2:3]
	s_mov_b32 m0, s16
	s_mov_b64 s[2:3], 0x4903000
	v_readfirstlane_b32 s17, v4
	v_add_u32_e32 v4, 0x4000, v6
	global_load_lds_dwordx4 v[2:3], off
	v_lshl_add_u64 v[2:3], v[134:135], 0, s[2:3]
	s_mov_b32 m0, s17
	s_mov_b64 s[2:3], 0x288000
	v_readfirstlane_b32 s18, v4
	v_add_u32_e32 v4, 0xc000, v6
	global_load_lds_dwordx4 v[2:3], off
	v_lshl_add_u64 v[2:3], v[132:133], 0, s[2:3]
	s_mov_b32 m0, s18
	s_mov_b64 s[2:3], 0x4904000
	v_readfirstlane_b32 s19, v4
	v_add_u32_e32 v4, 0x5000, v6
	global_load_lds_dwordx4 v[2:3], off
	v_lshl_add_u64 v[2:3], v[134:135], 0, s[2:3]
	s_mov_b32 m0, s19
	s_mov_b64 s[2:3], 0x28a000
	v_readfirstlane_b32 s20, v4
	v_add_u32_e32 v4, 0xd000, v6
	global_load_lds_dwordx4 v[2:3], off
	v_lshl_add_u64 v[2:3], v[132:133], 0, s[2:3]
	s_mov_b32 m0, s20
	s_mov_b64 s[2:3], 0x4905000
	v_readfirstlane_b32 s21, v4
	v_add_u32_e32 v4, 0x6000, v6
	global_load_lds_dwordx4 v[2:3], off
	v_lshl_add_u64 v[2:3], v[134:135], 0, s[2:3]
	s_mov_b32 m0, s21
	s_mov_b64 s[2:3], 0x28c000
	v_readfirstlane_b32 s22, v4
	v_add_u32_e32 v4, 0xe000, v6
	global_load_lds_dwordx4 v[2:3], off
	v_lshl_add_u64 v[2:3], v[132:133], 0, s[2:3]
	s_mov_b32 m0, s22
	s_mov_b64 s[2:3], 0x4906000
	v_readfirstlane_b32 s23, v4
	v_add_u32_e32 v4, 0x7000, v6
	global_load_lds_dwordx4 v[2:3], off
	v_lshl_add_u64 v[2:3], v[134:135], 0, s[2:3]
	s_mov_b32 m0, s23
	s_mov_b64 s[2:3], 0x28e000
	v_readfirstlane_b32 s24, v4
	global_load_lds_dwordx4 v[2:3], off
	v_lshl_add_u64 v[2:3], v[132:133], 0, s[2:3]
	s_mov_b32 m0, s24
	s_mov_b64 s[2:3], 0x4907000
	global_load_lds_dwordx4 v[2:3], off
	v_lshl_add_u64 v[2:3], v[134:135], 0, s[2:3]
	s_lshl_b32 s0, s0, 9
	s_lshl_b32 s2, s26, 7
	s_or_b32 s0, s0, s2
	s_ashr_i32 s1, s0, 31
	s_lshl_b64 s[0:1], s[0:1], 12
	s_lshl_b32 s3, s27, 2
	v_add_u32_e32 v4, 0xf000, v6
	s_or_b32 s3, s0, s3
	v_readfirstlane_b32 s25, v4
	s_add_u32 s6, s6, s3
	s_mov_b32 m0, s25
	s_addc_u32 s7, s7, s1
	v_and_b32_e32 v130, 0x1f0, v1
	v_lshlrev_b32_e32 v1, 7, v0
	global_load_lds_dwordx4 v[2:3], off
	v_lshlrev_b32_e32 v28, 5, v0
	v_lshl_add_u64 v[2:3], s[6:7], 0, v[130:131]
	v_and_b32_e32 v130, 0x7000, v1
	s_movk_i32 s0, 0x3c00
	v_mov_b32_e32 v1, 0x2000
	v_bitop3_b32 v1, v28, s0, v1 bitop3:0xc8
	v_lshl_add_u64 v[4:5], v[2:3], 0, v[130:131]
	v_lshlrev_b32_e32 v130, 2, v1
	s_movk_i32 s0, 0x5c00
	v_mov_b32_e32 v1, 0x4000
	v_bitop3_b32 v1, v28, s0, v1 bitop3:0xc8
	v_lshl_add_u64 v[6:7], v[2:3], 0, v[130:131]
	v_lshlrev_b32_e32 v130, 2, v1
	s_movk_i32 s0, 0x7c00
	v_mov_b32_e32 v1, 0x6000
	v_bitop3_b32 v1, v28, s0, v1 bitop3:0xc8
	v_lshl_add_u64 v[8:9], v[2:3], 0, v[130:131]
	v_lshlrev_b32_e32 v130, 2, v1
	s_mov_b32 s0, 0xbc00
	v_mov_b32_e32 v1, 0xa000
	v_bitop3_b32 v1, v28, s0, v1 bitop3:0xc8
	v_lshl_add_u64 v[10:11], v[2:3], 0, v[130:131]
	v_lshlrev_b32_e32 v130, 2, v1
	s_mov_b32 s0, 0xdc00
	v_mov_b32_e32 v1, 0xc000
	v_bitop3_b32 v1, v28, s0, v1 bitop3:0xc8
	v_lshl_add_u64 v[12:13], v[2:3], 0, v[130:131]
	v_lshlrev_b32_e32 v130, 2, v1
	s_mov_b32 s0, 0xfc00
	v_mov_b32_e32 v1, 0xe000
	v_bitop3_b32 v1, v28, s0, v1 bitop3:0xc8
	v_lshl_add_u64 v[14:15], v[2:3], 0, v[130:131]
	v_lshlrev_b32_e32 v130, 2, v1
	s_mov_b32 s0, 0x13c00
	v_mov_b32_e32 v1, 0x12000
	v_bitop3_b32 v1, v28, s0, v1 bitop3:0xc8
	v_lshl_add_u64 v[16:17], v[2:3], 0, v[130:131]
	v_lshlrev_b32_e32 v130, 2, v1
	s_mov_b32 s0, 0x15c00
	v_mov_b32_e32 v1, 0x14000
	v_bitop3_b32 v1, v28, s0, v1 bitop3:0xc8
	v_lshl_add_u64 v[18:19], v[2:3], 0, v[130:131]
	v_lshlrev_b32_e32 v130, 2, v1
	s_mov_b32 s0, 0x17c00
	v_mov_b32_e32 v1, 0x16000
	v_bitop3_b32 v1, v28, s0, v1 bitop3:0xc8
	v_lshl_add_u64 v[20:21], v[2:3], 0, v[130:131]
	v_lshlrev_b32_e32 v130, 2, v1
	s_mov_b32 s0, 0x1bc00
	v_mov_b32_e32 v1, 0x1a000
	v_bitop3_b32 v1, v28, s0, v1 bitop3:0xc8
	v_lshl_add_u64 v[22:23], v[2:3], 0, v[130:131]
	v_lshlrev_b32_e32 v130, 2, v1
	s_mov_b32 s0, 0x1dc00
	v_mov_b32_e32 v1, 0x1c000
	v_bitop3_b32 v1, v28, s0, v1 bitop3:0xc8
	v_lshl_add_u64 v[24:25], v[2:3], 0, v[130:131]
	v_lshlrev_b32_e32 v130, 2, v1
	s_mov_b32 s0, 0x1fc00
	v_mov_b32_e32 v1, 0x1e000
	v_bitop3_b32 v1, v28, s0, v1 bitop3:0xc8
	s_mov_b32 s0, 0x20000
	global_load_dwordx4 v[126:129], v[4:5], off nt
	global_load_dwordx4 v[122:125], v[6:7], off nt
	global_load_dwordx4 v[114:117], v[8:9], off nt
	global_load_dwordx4 v[110:113], v[10:11], off nt
	v_add_co_u32_e32 v6, vcc, s0, v4
	s_mov_b32 s0, 0x40000
	s_nop 0
	v_addc_co_u32_e32 v7, vcc, 0, v5, vcc
	v_add_co_u32_e32 v8, vcc, s0, v4
	s_mov_b32 s0, 0x60000
	s_nop 0
	v_addc_co_u32_e32 v9, vcc, 0, v5, vcc
	v_lshl_add_u64 v[26:27], v[2:3], 0, v[130:131]
	v_lshlrev_b32_e32 v130, 2, v1
	v_add_co_u32_e32 v4, vcc, s0, v4
	v_lshl_add_u64 v[2:3], v[2:3], 0, v[130:131]
	global_load_dwordx4 v[106:109], v[12:13], off nt
	global_load_dwordx4 v[102:105], v[14:15], off nt
	global_load_dwordx4 v[94:97], v[16:17], off nt
	global_load_dwordx4 v[90:93], v[18:19], off nt
	v_addc_co_u32_e32 v5, vcc, 0, v5, vcc
	global_load_dwordx4 v[86:89], v[20:21], off nt
	global_load_dwordx4 v[82:85], v[22:23], off nt
	global_load_dwordx4 v[98:101], v[8:9], off nt
	global_load_dwordx4 v[78:81], v[4:5], off nt
	global_load_dwordx4 v[74:77], v[24:25], off nt
	global_load_dwordx4 v[70:73], v[26:27], off nt
	global_load_dwordx4 v[118:121], v[6:7], off nt
	global_load_dwordx4 v[66:69], v[2:3], off nt
	v_and_b32_e32 v1, 31, v0
	v_or_b32_e32 v2, v136, v1
	v_lshl_add_u32 v137, v2, 8, 0
	v_lshlrev_b32_e32 v2, 8, v0
	v_bfe_u32 v130, v0, 5, 1
	v_and_b32_e32 v2, 0x5f00, v2
	v_lshlrev_b32_e32 v171, 1, v130
	v_add_u32_e32 v170, 0, v2
	v_bitop3_b32 v2, v171, v0, 15 bitop3:0x78
	v_and_b32_e32 v172, 15, v0
	v_lshlrev_b32_e32 v10, 4, v2
	v_bitop3_b32 v2, v171, v172, 1 bitop3:0x36
	v_lshlrev_b32_e32 v11, 4, v2
	s_waitcnt vmcnt(16) lgkmcnt(0)
	s_barrier
	v_add_u32_e32 v173, v137, v10
	v_add_u32_e32 v176, v170, v11
	v_add_u32_e32 v174, v137, v11
	ds_read_b128 v[2:5], v173
	ds_read_b128 v[6:9], v174
	ds_read_b128 v[14:17], v176 offset:32768
	v_add_u32_e32 v175, v170, v10
	ds_read_b128 v[10:13], v175 offset:32768
	ds_read_b128 v[18:21], v175 offset:40960
	ds_read_b128 v[22:25], v176 offset:40960
	ds_read_b128 v[26:29], v173 offset:8192
	ds_read_b128 v[30:33], v174 offset:8192
	v_bitop3_b32 v50, v171, v172, 4 bitop3:0x36
	v_bitop3_b32 v51, v171, v172, 5 bitop3:0x36
	v_lshlrev_b32_e32 v50, 4, v50
	v_lshlrev_b32_e32 v51, 4, v51
	s_waitcnt lgkmcnt(0)
	v_mfma_f32_32x32x64_f8f6f4 v[34:49], v[2:9], v[10:17], 0
	v_add_u32_e32 v177, v137, v50
	v_add_u32_e32 v178, v137, v51
	v_add_u32_e32 v179, v170, v50
	v_add_u32_e32 v180, v170, v51
	ds_read_b128 v[138:141], v177
	ds_read_b128 v[142:145], v178
	ds_read_b128 v[150:153], v180 offset:32768
	ds_read_b128 v[146:149], v179 offset:32768
	ds_read_b128 v[154:157], v179 offset:40960
	ds_read_b128 v[158:161], v180 offset:40960
	ds_read_b128 v[162:165], v177 offset:8192
	ds_read_b128 v[166:169], v178 offset:8192
	s_mov_b64 s[6:7], 0x280100
	s_mov_b32 m0, s5
	v_lshl_or_b32 v130, v130, 2, v136
	v_mul_u32_u24_e32 v130, 0x210, v130
	s_mov_b32 s0, 0x3a800000
	v_mfma_f32_32x32x64_f8f6f4 v[50:65], v[2:9], v[18:25], 0
	v_mfma_f32_32x32x64_f8f6f4 v[2:17], v[26:33], v[10:17], 0
	v_mfma_f32_32x32x64_f8f6f4 v[18:33], v[26:33], v[18:25], 0
	s_waitcnt lgkmcnt(0)
	v_mfma_f32_32x32x64_f8f6f4 v[34:49], v[138:145], v[146:153], v[34:49]
	v_mfma_f32_32x32x64_f8f6f4 v[50:65], v[138:145], v[154:161], v[50:65]
	v_bitop3_b32 v138, v171, v172, 8 bitop3:0x36
	v_mfma_f32_32x32x64_f8f6f4 v[2:17], v[162:169], v[146:153], v[2:17]
	v_lshlrev_b32_e32 v146, 4, v138
	v_bitop3_b32 v138, v171, v172, 9 bitop3:0x36
	v_lshlrev_b32_e32 v147, 4, v138
	v_add_u32_e32 v181, v137, v146
	v_add_u32_e32 v182, v137, v147
	ds_read_b128 v[138:141], v181
	ds_read_b128 v[142:145], v182
	v_add_u32_e32 v184, v170, v147
	v_add_u32_e32 v183, v170, v146
	v_mfma_f32_32x32x64_f8f6f4 v[18:33], v[162:169], v[154:161], v[18:33]
	ds_read_b128 v[150:153], v184 offset:32768
	ds_read_b128 v[146:149], v183 offset:32768
	ds_read_b128 v[154:157], v183 offset:40960
	ds_read_b128 v[158:161], v184 offset:40960
	ds_read_b128 v[162:165], v181 offset:8192
	ds_read_b128 v[166:169], v182 offset:8192
	s_waitcnt lgkmcnt(0)
	v_mfma_f32_32x32x64_f8f6f4 v[34:49], v[138:145], v[146:153], v[34:49]
	v_mfma_f32_32x32x64_f8f6f4 v[50:65], v[138:145], v[154:161], v[50:65]
	v_bitop3_b32 v138, v171, v172, 12 bitop3:0x36
	v_bitop3_b32 v139, v171, v172, 13 bitop3:0x36
	v_mfma_f32_32x32x64_f8f6f4 v[2:17], v[162:169], v[146:153], v[2:17]
	v_lshlrev_b32_e32 v146, 4, v138
	v_lshlrev_b32_e32 v147, 4, v139
	v_add_u32_e32 v171, v137, v146
	v_add_u32_e32 v137, v137, v147
	ds_read_b128 v[138:141], v171
	ds_read_b128 v[142:145], v137
	v_add_u32_e32 v172, v170, v146
	v_add_u32_e32 v170, v170, v147
	v_mfma_f32_32x32x64_f8f6f4 v[18:33], v[162:169], v[154:161], v[18:33]
	ds_read_b128 v[150:153], v170 offset:32768
	ds_read_b128 v[146:149], v172 offset:32768
	ds_read_b128 v[154:157], v172 offset:40960
	ds_read_b128 v[158:161], v170 offset:40960
	ds_read_b128 v[162:165], v171 offset:8192
	ds_read_b128 v[166:169], v137 offset:8192
	s_waitcnt lgkmcnt(0)
	s_barrier
	s_waitcnt lgkmcnt(0)
	v_mfma_f32_32x32x64_f8f6f4 v[34:49], v[138:145], v[146:153], v[34:49]
	v_mfma_f32_32x32x64_f8f6f4 v[50:65], v[138:145], v[154:161], v[50:65]
	v_lshl_add_u64 v[138:139], v[132:133], 0, s[6:7]
	s_mov_b64 s[6:7], 0x4d00000
	global_load_lds_dwordx4 v[138:139], off
	v_lshl_add_u64 v[138:139], v[134:135], 0, s[6:7]
	s_mov_b32 m0, s4
	s_mov_b64 s[4:5], 0x282100
	global_load_lds_dwordx4 v[138:139], off
	v_lshl_add_u64 v[138:139], v[132:133], 0, s[4:5]
	s_mov_b32 m0, s12
	s_mov_b64 s[4:5], 0x4d01000
	global_load_lds_dwordx4 v[138:139], off
	v_lshl_add_u64 v[138:139], v[134:135], 0, s[4:5]
	s_mov_b32 m0, s13
	s_mov_b64 s[4:5], 0x284100
	global_load_lds_dwordx4 v[138:139], off
	v_lshl_add_u64 v[138:139], v[132:133], 0, s[4:5]
	s_mov_b32 m0, s14
	s_mov_b64 s[4:5], 0x4d02000
	global_load_lds_dwordx4 v[138:139], off
	v_lshl_add_u64 v[138:139], v[134:135], 0, s[4:5]
	s_mov_b32 m0, s15
	s_mov_b64 s[4:5], 0x286100
	global_load_lds_dwordx4 v[138:139], off
	v_lshl_add_u64 v[138:139], v[132:133], 0, s[4:5]
	s_mov_b32 m0, s16
	s_mov_b64 s[4:5], 0x4d03000
	global_load_lds_dwordx4 v[138:139], off
	v_lshl_add_u64 v[138:139], v[134:135], 0, s[4:5]
	s_mov_b32 m0, s17
	s_mov_b64 s[4:5], 0x288100
	global_load_lds_dwordx4 v[138:139], off
	v_lshl_add_u64 v[138:139], v[132:133], 0, s[4:5]
	s_mov_b32 m0, s18
	s_mov_b64 s[4:5], 0x4d04000
	global_load_lds_dwordx4 v[138:139], off
	v_lshl_add_u64 v[138:139], v[134:135], 0, s[4:5]
	s_mov_b32 m0, s19
	s_mov_b64 s[4:5], 0x28a100
	global_load_lds_dwordx4 v[138:139], off
	v_lshl_add_u64 v[138:139], v[132:133], 0, s[4:5]
	s_mov_b32 m0, s20
	s_mov_b64 s[4:5], 0x4d05000
	global_load_lds_dwordx4 v[138:139], off
	v_lshl_add_u64 v[138:139], v[134:135], 0, s[4:5]
	s_mov_b32 m0, s21
	s_mov_b64 s[4:5], 0x28c100
	v_mfma_f32_32x32x64_f8f6f4 v[2:17], v[162:169], v[146:153], v[2:17]
	global_load_lds_dwordx4 v[138:139], off
	v_lshl_add_u64 v[138:139], v[132:133], 0, s[4:5]
	s_mov_b32 m0, s22
	s_mov_b64 s[4:5], 0x4d06000
	global_load_lds_dwordx4 v[138:139], off
	v_lshl_add_u64 v[138:139], v[134:135], 0, s[4:5]
	s_mov_b32 m0, s23
	s_mov_b64 s[4:5], 0x28e100
	global_load_lds_dwordx4 v[138:139], off
	v_lshl_add_u64 v[132:133], v[132:133], 0, s[4:5]
	s_mov_b32 m0, s24
	s_mov_b64 s[4:5], 0x4d07000
	v_mfma_f32_32x32x64_f8f6f4 v[18:33], v[162:169], v[154:161], v[18:33]
	global_load_lds_dwordx4 v[132:133], off
	v_lshl_add_u64 v[132:133], v[134:135], 0, s[4:5]
	s_mov_b32 m0, s25
	s_movk_i32 s4, 0x210
	global_load_lds_dwordx4 v[132:133], off
	s_waitcnt vmcnt(0) lgkmcnt(0)
	s_barrier
	ds_read_b128 v[142:145], v174
	ds_read_b128 v[138:141], v173
	ds_read_b128 v[150:153], v176 offset:32768
	ds_read_b128 v[146:149], v175 offset:32768
	ds_read_b128 v[154:157], v175 offset:40960
	ds_read_b128 v[158:161], v176 offset:40960
	ds_read_b128 v[162:165], v173 offset:8192
	ds_read_b128 v[166:169], v174 offset:8192
	s_waitcnt lgkmcnt(4)
	v_mfma_f32_32x32x64_f8f6f4 v[34:49], v[138:145], v[146:153], v[34:49]
	v_lshlrev_b32_e32 v132, 2, v0
	v_and_b32_e32 v132, 0x17c, v132
	v_add3_u32 v130, 0, v132, v130
	v_add_u32_e32 v132, 0x400, v130
	s_add_u32 s6, s10, s3
	s_addc_u32 s7, s11, s1
	s_waitcnt lgkmcnt(2)
	v_mfma_f32_32x32x64_f8f6f4 v[50:65], v[138:145], v[154:161], v[50:65]
	s_waitcnt lgkmcnt(0)
	v_mfma_f32_32x32x64_f8f6f4 v[2:17], v[162:169], v[146:153], v[2:17]
	v_mfma_f32_32x32x64_f8f6f4 v[18:33], v[162:169], v[154:161], v[18:33]
	ds_read_b128 v[142:145], v178
	ds_read_b128 v[138:141], v177
	ds_read_b128 v[150:153], v180 offset:32768
	ds_read_b128 v[146:149], v179 offset:32768
	ds_read_b128 v[154:157], v179 offset:40960
	ds_read_b128 v[158:161], v180 offset:40960
	ds_read_b128 v[162:165], v177 offset:8192
	ds_read_b128 v[166:169], v178 offset:8192
	s_waitcnt lgkmcnt(4)
	v_mfma_f32_32x32x64_f8f6f4 v[34:49], v[138:145], v[146:153], v[34:49]
	s_waitcnt lgkmcnt(2)
	v_mfma_f32_32x32x64_f8f6f4 v[50:65], v[138:145], v[154:161], v[50:65]
	s_waitcnt lgkmcnt(0)
	v_mfma_f32_32x32x64_f8f6f4 v[2:17], v[162:169], v[146:153], v[2:17]
	v_mfma_f32_32x32x64_f8f6f4 v[18:33], v[162:169], v[154:161], v[18:33]
	ds_read_b128 v[142:145], v182
	ds_read_b128 v[138:141], v181
	ds_read_b128 v[150:153], v184 offset:32768
	ds_read_b128 v[146:149], v183 offset:32768
	ds_read_b128 v[154:157], v183 offset:40960
	ds_read_b128 v[158:161], v184 offset:40960
	ds_read_b128 v[162:165], v181 offset:8192
	ds_read_b128 v[166:169], v182 offset:8192
	s_waitcnt lgkmcnt(4)
	v_mfma_f32_32x32x64_f8f6f4 v[34:49], v[138:145], v[146:153], v[34:49]
	s_waitcnt lgkmcnt(2)
	v_mfma_f32_32x32x64_f8f6f4 v[50:65], v[138:145], v[154:161], v[50:65]
	s_waitcnt lgkmcnt(0)
	v_mfma_f32_32x32x64_f8f6f4 v[2:17], v[162:169], v[146:153], v[2:17]
	v_mfma_f32_32x32x64_f8f6f4 v[18:33], v[162:169], v[154:161], v[18:33]
	ds_read_b128 v[142:145], v137
	ds_read_b128 v[138:141], v171
	ds_read_b128 v[150:153], v170 offset:32768
	ds_read_b128 v[146:149], v172 offset:32768
	ds_read_b128 v[154:157], v172 offset:40960
	ds_read_b128 v[158:161], v170 offset:40960
	ds_read_b128 v[162:165], v171 offset:8192
	ds_read_b128 v[166:169], v137 offset:8192
	s_waitcnt lgkmcnt(0)
	s_barrier
	v_mfma_f32_32x32x64_f8f6f4 v[34:49], v[138:145], v[146:153], v[34:49]
	v_mfma_f32_32x32x64_f8f6f4 v[50:65], v[138:145], v[154:161], v[50:65]
	s_nop 15
	s_nop 2
	ds_write2_b32 v132, v36, v52 offset0:8 offset1:40
	ds_write2_b32 v132, v37, v53 offset0:140 offset1:172
	v_mfma_f32_32x32x64_f8f6f4 v[2:17], v[162:169], v[146:153], v[2:17]
	v_add_u32_e32 v36, 0x1000, v130
	ds_write2_b32 v36, v38, v54 offset0:32 offset1:64
	ds_write2_b32 v36, v39, v55 offset0:164 offset1:196
	v_add_u32_e32 v36, 0x1400, v130
	ds_write2_b32 v36, v40, v56 offset0:40 offset1:72
	ds_write2_b32 v36, v41, v57 offset0:172 offset1:204
	v_add_u32_e32 v36, 0x2000, v130
	ds_write2_b32 v36, v42, v58 offset0:64 offset1:96
	ds_write2_b32 v36, v43, v59 offset0:196 offset1:228
	v_add_u32_e32 v36, 0x2400, v130
	ds_write2_b32 v36, v44, v60 offset0:72 offset1:104
	ds_write2_b32 v36, v45, v61 offset0:204 offset1:236
	v_add_u32_e32 v36, 0x3000, v130
	ds_write2_b32 v36, v46, v62 offset0:96 offset1:128
	v_add_u32_e32 v36, 0x3200, v130
	ds_write2_b32 v36, v47, v63 offset0:100 offset1:132
	v_add_u32_e32 v36, 0x3400, v130
	ds_write2_b32 v36, v48, v64 offset0:104 offset1:136
	v_add_u32_e32 v36, 0x3600, v130
	v_mfma_f32_32x32x64_f8f6f4 v[18:33], v[162:169], v[154:161], v[18:33]
	ds_write2_b32 v36, v49, v65 offset0:108 offset1:140
	ds_write2_b32 v130, v34, v50 offset1:32
	ds_write2_b32 v130, v35, v51 offset0:132 offset1:164
	v_add_u32_e32 v34, 0x4000, v130
	s_nop 15
	ds_write2_b32 v34, v2, v18 offset0:128 offset1:160
	v_add_u32_e32 v2, 0x4400, v130
	ds_write2_b32 v2, v3, v19 offset0:4 offset1:36
	ds_write2_b32 v2, v4, v20 offset0:136 offset1:168
	v_add_u32_e32 v2, 0x4800, v130
	ds_write2_b32 v2, v5, v21 offset0:12 offset1:44
	v_add_u32_e32 v2, 0x5000, v130
	ds_write2_b32 v2, v6, v22 offset0:160 offset1:192
	v_add_u32_e32 v2, 0x5400, v130
	ds_write2_b32 v2, v7, v23 offset0:36 offset1:68
	ds_write2_b32 v2, v8, v24 offset0:168 offset1:200
	v_add_u32_e32 v2, 0x5800, v130
	ds_write2_b32 v2, v9, v25 offset0:44 offset1:76
	v_add_u32_e32 v2, 0x6000, v130
	ds_write2_b32 v2, v10, v26 offset0:192 offset1:224
	v_add_u32_e32 v2, 0x6400, v130
	ds_write2_b32 v2, v11, v27 offset0:68 offset1:100
	ds_write2_b32 v2, v12, v28 offset0:200 offset1:232
	v_add_u32_e32 v2, 0x6800, v130
	ds_write2_b32 v2, v13, v29 offset0:76 offset1:108
	v_add_u32_e32 v2, 0x7200, v130
	ds_write2_b32 v2, v14, v30 offset0:96 offset1:128
	v_add_u32_e32 v2, 0x7400, v130
	ds_write2_b32 v2, v15, v31 offset0:100 offset1:132
	v_add_u32_e32 v2, 0x7600, v130
	ds_write2_b32 v2, v16, v32 offset0:104 offset1:136
	v_add_u32_e32 v2, 0x7800, v130
	v_lshrrev_b32_e32 v21, 5, v0
	ds_write2_b32 v2, v17, v33 offset0:108 offset1:140
	v_or_b32_e32 v2, s2, v21
	v_lshlrev_b32_e32 v3, 2, v2
	s_waitcnt lgkmcnt(0)
	s_barrier
	global_load_dword v2, v3, s[8:9]
	v_or_b32_e32 v4, 0x100, v0
	v_lshrrev_b32_e32 v23, 5, v4
	v_or_b32_e32 v4, s2, v23
	v_lshlrev_b32_e32 v4, 2, v4
	global_load_dword v20, v4, s[8:9]
	v_or_b32_e32 v4, 0x200, v0
	v_lshrrev_b32_e32 v25, 5, v4
	v_or_b32_e32 v4, s2, v25
	v_lshlrev_b32_e32 v4, 2, v4
	global_load_dword v22, v4, s[8:9]
	v_or_b32_e32 v4, 0x300, v0
	v_lshrrev_b32_e32 v27, 5, v4
	v_or_b32_e32 v4, s2, v27
	v_lshlrev_b32_e32 v4, 2, v4
	global_load_dword v24, v4, s[8:9]
	global_load_dword v26, v3, s[8:9] offset:128
	v_or_b32_e32 v12, 0x500, v0
	v_lshlrev_b32_e32 v130, 4, v1
	v_lshrrev_b32_e32 v31, 5, v12
	v_add_u32_e32 v1, 0, v130
	v_or_b32_e32 v12, s2, v31
	v_mad_u32_u24 v29, v21, s4, v1
	v_lshlrev_b32_e32 v12, 2, v12
	ds_read_b128 v[4:7], v29
	ds_read_b128 v[8:11], v29 offset:16896
	global_load_dword v28, v12, s[8:9]
	s_waitcnt lgkmcnt(1)
	v_pk_fma_f32 v[6:7], v[6:7], s[0:1], v[128:129] op_sel_hi:[1,0,1]
	v_pk_fma_f32 v[12:13], v[4:5], s[0:1], v[126:127] op_sel_hi:[1,0,1]
	global_load_dword v30, v3, s[8:9] offset:256
	global_load_dword v4, v3, s[8:9] offset:384
	s_waitcnt vmcnt(7)
	v_pk_add_f32 v[14:15], v[6:7], v[2:3] op_sel_hi:[1,0]
	v_pk_add_f32 v[12:13], v[12:13], v[2:3] op_sel_hi:[1,0]
	v_mad_u32_u24 v2, v23, s4, v1
	ds_read_b128 v[16:19], v2
	v_or_b32_e32 v2, 0x600, v0
	v_lshrrev_b32_e32 v5, 5, v2
	v_or_b32_e32 v2, s2, v5
	v_lshlrev_b32_e32 v2, 2, v2
	global_load_dword v32, v2, s[8:9]
	v_lshl_add_u64 v[2:3], s[6:7], 0, v[130:131]
	v_lshlrev_b32_e32 v130, 12, v21
	v_lshl_add_u64 v[6:7], v[2:3], 0, v[130:131]
	global_store_dwordx4 v[6:7], v[12:15], off nt
	s_waitcnt lgkmcnt(0)
	v_pk_fma_f32 v[6:7], v[18:19], s[0:1], v[124:125] op_sel_hi:[1,0,1]
	s_waitcnt vmcnt(8)
	v_pk_add_f32 v[14:15], v[6:7], v[20:21] op_sel_hi:[1,0]
	v_mad_u32_u24 v6, v25, s4, v1
	v_pk_fma_f32 v[12:13], v[16:17], s[0:1], v[122:123] op_sel_hi:[1,0,1]
	ds_read_b128 v[16:19], v6
	v_lshlrev_b32_e32 v6, 12, v23
	v_mov_b32_e32 v7, v131
	v_pk_add_f32 v[12:13], v[12:13], v[20:21] op_sel_hi:[1,0]
	v_lshl_add_u64 v[6:7], v[2:3], 0, v[6:7]
	global_store_dwordx4 v[6:7], v[12:15], off nt
	s_waitcnt lgkmcnt(0)
	v_pk_fma_f32 v[6:7], v[18:19], s[0:1], v[116:117] op_sel_hi:[1,0,1]
	v_or_b32_e32 v12, 0x700, v0
	v_lshrrev_b32_e32 v21, 5, v12
	v_or_b32_e32 v12, s2, v21
	v_lshlrev_b32_e32 v12, 2, v12
	s_waitcnt vmcnt(8)
	v_pk_add_f32 v[14:15], v[6:7], v[22:23] op_sel_hi:[1,0]
	v_mad_u32_u24 v6, v27, s4, v1
	global_load_dword v20, v12, s[8:9]
	v_pk_fma_f32 v[12:13], v[16:17], s[0:1], v[114:115] op_sel_hi:[1,0,1]
	ds_read_b128 v[16:19], v6
	v_lshlrev_b32_e32 v6, 12, v25
	v_mov_b32_e32 v7, v131
	v_pk_add_f32 v[12:13], v[12:13], v[22:23] op_sel_hi:[1,0]
	v_lshl_add_u64 v[6:7], v[2:3], 0, v[6:7]
	global_store_dwordx4 v[6:7], v[12:15], off nt
	s_waitcnt lgkmcnt(0)
	v_pk_fma_f32 v[6:7], v[18:19], s[0:1], v[112:113] op_sel_hi:[1,0,1]
	v_pk_fma_f32 v[12:13], v[16:17], s[0:1], v[110:111] op_sel_hi:[1,0,1]
	v_or_b32_e32 v16, 0x900, v0
	v_lshrrev_b32_e32 v19, 5, v16
	v_or_b32_e32 v16, s2, v19
	s_waitcnt vmcnt(9)
	v_pk_add_f32 v[14:15], v[6:7], v[24:25] op_sel_hi:[1,0]
	v_lshlrev_b32_e32 v6, 12, v27
	v_mov_b32_e32 v7, v131
	v_lshlrev_b32_e32 v16, 2, v16
	v_pk_add_f32 v[12:13], v[12:13], v[24:25] op_sel_hi:[1,0]
	global_load_dword v18, v16, s[8:9]
	v_lshl_add_u64 v[6:7], v[2:3], 0, v[6:7]
	global_store_dwordx4 v[6:7], v[12:15], off nt
	v_pk_fma_f32 v[6:7], v[10:11], s[0:1], v[120:121] op_sel_hi:[1,0,1]
	v_pk_fma_f32 v[10:11], v[8:9], s[0:1], v[118:119] op_sel_hi:[1,0,1]
	s_waitcnt vmcnt(10)
	v_pk_add_f32 v[8:9], v[6:7], v[26:27] op_sel_hi:[1,0]
	v_or_b32_e32 v6, 0xa00, v0
	v_lshrrev_b32_e32 v23, 5, v6
	v_or_b32_e32 v6, s2, v23
	v_lshlrev_b32_e32 v6, 2, v6
	global_load_dword v22, v6, s[8:9]
	v_pk_add_f32 v[6:7], v[10:11], v[26:27] op_sel_hi:[1,0]
	v_mad_u32_u24 v10, v31, s4, v1
	v_or_b32_e32 v16, 0xb00, v0
	ds_read_b128 v[10:13], v10
	v_lshrrev_b32_e32 v25, 5, v16
	v_or_b32_e32 v16, s2, v25
	v_lshlrev_b32_e32 v16, 2, v16
	v_or_b32_e32 v14, 0x20000, v130
	v_mov_b32_e32 v15, v131
	global_load_dword v24, v16, s[8:9]
	v_lshl_add_u64 v[14:15], v[2:3], 0, v[14:15]
	global_store_dwordx4 v[14:15], v[6:9], off nt
	s_waitcnt lgkmcnt(0)
	v_pk_fma_f32 v[10:11], v[10:11], s[0:1], v[106:107] op_sel_hi:[1,0,1]
	v_lshlrev_b32_e32 v14, 12, v5
	v_pk_fma_f32 v[6:7], v[12:13], s[0:1], v[108:109] op_sel_hi:[1,0,1]
	v_mov_b32_e32 v15, v131
	s_waitcnt vmcnt(12)
	v_pk_add_f32 v[8:9], v[6:7], v[28:29] op_sel_hi:[1,0]
	v_pk_add_f32 v[6:7], v[10:11], v[28:29] op_sel_hi:[1,0]
	v_lshlrev_b32_e32 v10, 12, v31
	v_mov_b32_e32 v11, v131
	v_lshl_add_u64 v[10:11], v[2:3], 0, v[10:11]
	global_store_dwordx4 v[10:11], v[6:9], off nt
	v_or_b32_e32 v10, 0xd00, v0
	v_lshrrev_b32_e32 v27, 5, v10
	v_or_b32_e32 v10, s2, v27
	v_lshlrev_b32_e32 v10, 2, v10
	global_load_dword v26, v10, s[8:9]
	v_mad_u32_u24 v6, v5, s4, v1
	ds_read_b128 v[6:9], v6
	v_or_b32_e32 v10, 0xe00, v0
	v_lshrrev_b32_e32 v31, 5, v10
	v_or_b32_e32 v10, s2, v31
	v_lshlrev_b32_e32 v10, 2, v10
	global_load_dword v28, v10, s[8:9]
	v_mad_u32_u24 v10, v21, s4, v1
	ds_read_b128 v[10:13], v10
	s_waitcnt lgkmcnt(1)
	v_pk_fma_f32 v[8:9], v[8:9], s[0:1], v[104:105] op_sel_hi:[1,0,1]
	v_pk_fma_f32 v[6:7], v[6:7], s[0:1], v[102:103] op_sel_hi:[1,0,1]
	v_or_b32_e32 v0, 0xf00, v0
	s_waitcnt vmcnt(12)
	v_pk_add_f32 v[8:9], v[8:9], v[32:33] op_sel_hi:[1,0]
	v_pk_add_f32 v[6:7], v[6:7], v[32:33] op_sel_hi:[1,0]
	v_lshrrev_b32_e32 v32, 5, v0
	v_or_b32_e32 v0, s2, v32
	v_lshlrev_b32_e32 v0, 2, v0
	global_load_dword v0, v0, s[8:9]
	v_lshl_add_u64 v[14:15], v[2:3], 0, v[14:15]
	global_store_dwordx4 v[14:15], v[6:9], off nt
	s_waitcnt lgkmcnt(0)
	v_pk_fma_f32 v[10:11], v[10:11], s[0:1], v[94:95] op_sel_hi:[1,0,1]
	v_lshlrev_b32_e32 v14, 12, v21
	v_pk_fma_f32 v[6:7], v[12:13], s[0:1], v[96:97] op_sel_hi:[1,0,1]
	v_mov_b32_e32 v15, v131
	s_waitcnt vmcnt(11)
	v_pk_add_f32 v[8:9], v[6:7], v[20:21] op_sel_hi:[1,0]
	v_pk_add_f32 v[6:7], v[10:11], v[20:21] op_sel_hi:[1,0]
	ds_read_b128 v[10:13], v29 offset:33792
	v_lshl_add_u64 v[14:15], v[2:3], 0, v[14:15]
	v_mad_u32_u24 v5, v19, s4, v1
	global_store_dwordx4 v[14:15], v[6:9], off nt
	ds_read_b128 v[14:17], v5
	s_waitcnt lgkmcnt(1)
	v_pk_fma_f32 v[12:13], v[12:13], s[0:1], v[100:101] op_sel_hi:[1,0,1]
	v_pk_fma_f32 v[10:11], v[10:11], s[0:1], v[98:99] op_sel_hi:[1,0,1]
	v_or_b32_e32 v20, 0x40000, v130
	v_mov_b32_e32 v21, v131
	v_pk_add_f32 v[12:13], v[12:13], v[30:31] op_sel_hi:[1,0]
	v_pk_add_f32 v[10:11], v[10:11], v[30:31] op_sel_hi:[1,0]
	v_lshl_add_u64 v[20:21], v[2:3], 0, v[20:21]
	global_store_dwordx4 v[20:21], v[10:13], off nt
	s_waitcnt lgkmcnt(0)
	v_pk_fma_f32 v[14:15], v[14:15], s[0:1], v[90:91] op_sel_hi:[1,0,1]
	v_mad_u32_u24 v5, v23, s4, v1
	v_pk_fma_f32 v[10:11], v[16:17], s[0:1], v[92:93] op_sel_hi:[1,0,1]
	ds_read_b128 v[6:9], v29 offset:50688
	s_waitcnt vmcnt(11)
	v_pk_add_f32 v[12:13], v[10:11], v[18:19] op_sel_hi:[1,0]
	v_pk_add_f32 v[10:11], v[14:15], v[18:19] op_sel_hi:[1,0]
	ds_read_b128 v[14:17], v5
	v_lshlrev_b32_e32 v18, 12, v19
	v_mov_b32_e32 v19, v131
	v_lshl_add_u64 v[18:19], v[2:3], 0, v[18:19]
	global_store_dwordx4 v[18:19], v[10:13], off nt
	s_waitcnt lgkmcnt(0)
	v_pk_fma_f32 v[14:15], v[14:15], s[0:1], v[86:87] op_sel_hi:[1,0,1]
	v_mad_u32_u24 v5, v25, s4, v1
	v_pk_fma_f32 v[10:11], v[16:17], s[0:1], v[88:89] op_sel_hi:[1,0,1]
	v_lshlrev_b32_e32 v18, 12, v23
	s_waitcnt vmcnt(10)
	v_pk_add_f32 v[12:13], v[10:11], v[22:23] op_sel_hi:[1,0]
	v_pk_add_f32 v[10:11], v[14:15], v[22:23] op_sel_hi:[1,0]
	ds_read_b128 v[14:17], v5
	v_mov_b32_e32 v19, v131
	v_lshl_add_u64 v[18:19], v[2:3], 0, v[18:19]
	global_store_dwordx4 v[18:19], v[10:13], off nt
	v_pk_fma_f32 v[8:9], v[8:9], s[0:1], v[80:81] op_sel_hi:[1,0,1]
	s_waitcnt lgkmcnt(0)
	v_pk_fma_f32 v[14:15], v[14:15], s[0:1], v[82:83] op_sel_hi:[1,0,1]
	v_pk_fma_f32 v[10:11], v[16:17], s[0:1], v[84:85] op_sel_hi:[1,0,1]
	v_or_b32_e32 v130, 0x60000, v130
	s_waitcnt vmcnt(10)
	v_pk_add_f32 v[12:13], v[10:11], v[24:25] op_sel_hi:[1,0]
	v_pk_add_f32 v[10:11], v[14:15], v[24:25] op_sel_hi:[1,0]
	v_lshlrev_b32_e32 v14, 12, v25
	v_mov_b32_e32 v15, v131
	v_lshl_add_u64 v[14:15], v[2:3], 0, v[14:15]
	global_store_dwordx4 v[14:15], v[10:13], off nt
	s_nop 1
	v_pk_fma_f32 v[12:13], v[6:7], s[0:1], v[78:79] op_sel_hi:[1,0,1]
	v_pk_add_f32 v[6:7], v[8:9], v[4:5] op_sel_hi:[1,0]
	v_mad_u32_u24 v5, v27, s4, v1
	ds_read_b128 v[8:11], v5
	v_pk_add_f32 v[4:5], v[12:13], v[4:5] op_sel_hi:[1,0]
	v_lshl_add_u64 v[12:13], v[2:3], 0, v[130:131]
	global_store_dwordx4 v[12:13], v[4:7], off nt
	v_lshlrev_b32_e32 v130, 12, v27
	s_waitcnt lgkmcnt(0)
	v_pk_fma_f32 v[12:13], v[8:9], s[0:1], v[74:75] op_sel_hi:[1,0,1]
	v_pk_fma_f32 v[4:5], v[10:11], s[0:1], v[76:77] op_sel_hi:[1,0,1]
	s_waitcnt vmcnt(9)
	v_pk_add_f32 v[6:7], v[4:5], v[26:27] op_sel_hi:[1,0]
	v_mad_u32_u24 v4, v31, s4, v1
	ds_read_b128 v[8:11], v4
	v_pk_add_f32 v[4:5], v[12:13], v[26:27] op_sel_hi:[1,0]
	v_lshl_add_u64 v[12:13], v[2:3], 0, v[130:131]
	v_mad_u32_u24 v1, v32, s4, v1
	global_store_dwordx4 v[12:13], v[4:7], off nt
	s_waitcnt lgkmcnt(0)
	v_pk_fma_f32 v[12:13], v[8:9], s[0:1], v[70:71] op_sel_hi:[1,0,1]
	v_lshlrev_b32_e32 v130, 12, v31
	v_pk_fma_f32 v[4:5], v[10:11], s[0:1], v[72:73] op_sel_hi:[1,0,1]
	ds_read_b128 v[8:11], v1
	s_waitcnt vmcnt(9)
	v_pk_add_f32 v[6:7], v[4:5], v[28:29] op_sel_hi:[1,0]
	v_pk_add_f32 v[4:5], v[12:13], v[28:29] op_sel_hi:[1,0]
	v_lshl_add_u64 v[12:13], v[2:3], 0, v[130:131]
	global_store_dwordx4 v[12:13], v[4:7], off nt
	s_waitcnt lgkmcnt(0)
	v_pk_fma_f32 v[8:9], v[8:9], s[0:1], v[66:67] op_sel_hi:[1,0,1]
	v_lshlrev_b32_e32 v130, 12, v32
	v_pk_fma_f32 v[4:5], v[10:11], s[0:1], v[68:69] op_sel_hi:[1,0,1]
	s_waitcnt vmcnt(9)
	v_pk_add_f32 v[6:7], v[4:5], v[0:1] op_sel_hi:[1,0]
	v_pk_add_f32 v[4:5], v[8:9], v[0:1] op_sel_hi:[1,0]
	v_lshl_add_u64 v[0:1], v[2:3], 0, v[130:131]
	global_store_dwordx4 v[0:1], v[4:7], off nt
	s_endpgm

	.amdhsa_kernel _Z11proj_kernelPKcPKfS2_Pf
		.amdhsa_group_segment_fixed_size 0
		.amdhsa_private_segment_fixed_size 0
		.amdhsa_kernarg_size 32
		.amdhsa_user_sgpr_count 2
		.amdhsa_user_sgpr_dispatch_ptr 0
		.amdhsa_user_sgpr_queue_ptr 0
		.amdhsa_user_sgpr_kernarg_segment_ptr 1
		.amdhsa_user_sgpr_dispatch_id 0
		.amdhsa_user_sgpr_kernarg_preload_length 0
		.amdhsa_user_sgpr_kernarg_preload_offset 0
		.amdhsa_user_sgpr_private_segment_size 0
		.amdhsa_uses_dynamic_stack 0
		.amdhsa_enable_private_segment 0
		.amdhsa_system_sgpr_workgroup_id_x 1
		.amdhsa_system_sgpr_workgroup_id_y 0
		.amdhsa_system_sgpr_workgroup_id_z 0
		.amdhsa_system_sgpr_workgroup_info 0
		.amdhsa_system_vgpr_workitem_id 0
		.amdhsa_next_free_vgpr 194
		.amdhsa_next_free_sgpr 28
		.amdhsa_accum_offset 196
		.amdhsa_reserve_vcc 1
		.amdhsa_float_round_mode_32 0
		.amdhsa_float_round_mode_16_64 0
		.amdhsa_float_denorm_mode_32 3
		.amdhsa_float_denorm_mode_16_64 3
		.amdhsa_dx10_clamp 1
		.amdhsa_ieee_mode 1
		.amdhsa_fp16_overflow 0
		.amdhsa_tg_split 0
		.amdhsa_exception_fp_ieee_invalid_op 0
		.amdhsa_exception_fp_denorm_src 0
		.amdhsa_exception_fp_ieee_div_zero 0
		.amdhsa_exception_fp_ieee_overflow 0
		.amdhsa_exception_fp_ieee_underflow 0
		.amdhsa_exception_fp_ieee_inexact 0
		.amdhsa_exception_int_div_zero 0
	.end_amdhsa_kernel

_Z13attn11_kernelILi4EEvPc:
	s_ashr_i32 s5, s2, 3
	s_load_dwordx2 s[12:13], s[0:1], 0x0
	s_lshr_b32 s4, s5, 29
	s_lshl_b32 s3, s2, 4
	s_add_i32 s6, s5, s4
	s_and_b32 s3, s3, 0x70
	s_ashr_i32 s4, s6, 3
	s_add_i32 s4, s3, s4
	s_and_b32 s3, s6, 0x1fffff8
	s_sub_i32 s3, s5, s3
	v_lshrrev_b32_e32 v1, 6, v0
	s_waitcnt lgkmcnt(0)
	s_add_u32 s14, s12, 0x2500000
	v_lshlrev_b32_e32 v192, 5, v1
	s_addc_u32 s15, s13, 0
	s_ashr_i32 s5, s4, 31
	s_mul_i32 s6, s4, 0x12000
	v_lshl_or_b32 v172, s3, 7, v192
	s_mul_hi_i32 s3, s4, 0x12000
	s_add_u32 s8, s14, s6
	s_addc_u32 s9, s15, s3
	s_add_u32 s16, s12, 0x3700000
	v_lshlrev_b32_e32 v169, 4, v0
	s_addc_u32 s17, s13, 0
	s_add_u32 s10, s16, s6
	v_add_u32_e32 v193, 0, v169
	v_lshrrev_b32_e32 v2, 2, v0
	v_bitop3_b32 v3, v169, 48, v0 bitop3:0x48
	s_addc_u32 s11, s17, s3
	s_mov_b64 s[46:47], s[8:9]
	s_mov_b64 s[48:49], s[10:11]
	s_mov_b64 s[50:51], s[14:15]
	s_mov_b64 s[52:53], s[16:17]
	v_readfirstlane_b32 s3, v193
	v_add_u32_e32 v4, 0x8000, v193
	v_lshl_or_b32 v170, v2, 6, v3
	v_mul_u32_u24_e32 v2, 0x480, v2
	v_mov_b32_e32 v171, 0
	s_mov_b32 m0, s3
	v_readfirstlane_b32 s3, v4
	v_add_u32_e32 v6, 0x2000, v193
	v_or_b32_e32 v2, v2, v3
	v_lshl_add_u64 v[174:175], s[8:9], 0, v[170:171]
	v_mov_b32_e32 v3, v171
	global_load_lds_dwordx4 v170, s[8:9]
	v_mov_b32_e32 v220, v170
	s_mov_b32 m0, s3
	s_mov_b64 s[8:9], 0x1000
	v_readfirstlane_b32 s6, v6
	v_add_u32_e32 v6, 0x4000, v193
	v_lshl_add_u64 v[176:177], s[10:11], 0, v[2:3]
	global_load_lds_dwordx4 v2, s[10:11]
	v_mov_b32_e32 v221, v2
	v_lshl_add_u64 v[4:5], v[174:175], 0, s[8:9]
	s_mov_b32 m0, s6
	s_mov_b64 s[10:11], 0x2000
	v_readfirstlane_b32 s6, v6
	v_add_u32_e32 v6, 0xa000, v193
	global_load_lds_dwordx4 v[4:5], off
	v_lshl_add_u64 v[4:5], v[174:175], 0, s[10:11]
	s_mov_b32 m0, s6
	v_readfirstlane_b32 s6, v6
	s_add_u32 s18, s12, 0x1500000
	global_load_lds_dwordx4 v[4:5], off
	v_lshl_add_u64 v[4:5], v[176:177], 0, 64
	s_mov_b32 m0, s6
	s_addc_u32 s19, s13, 0
	s_lshl_b64 s[20:21], s[4:5], 10
	v_ashrrev_i32_e32 v173, 31, v172
	v_and_b32_e32 v168, 31, v0
	global_load_lds_dwordx4 v[4:5], off
	v_lshl_add_u64 v[4:5], s[20:21], 0, v[172:173]
	v_or_b32_e32 v4, v4, v168
	v_lshlrev_b64 v[4:5], 6, v[4:5]
	v_lshl_add_u64 v[4:5], s[18:19], 0, v[4:5]
	v_and_b32_e32 v6, 32, v0
	v_mov_b32_e32 v7, v171
	v_lshl_add_u64 v[4:5], v[4:5], 0, v[6:7]
	global_load_dwordx4 v[152:155], v[4:5], off
	global_load_dwordx4 v[156:159], v[4:5], off offset:16
	v_and_b32_e32 v4, 60, v0
	v_lshlrev_b32_e32 v5, 2, v0
	s_add_u32 s0, s0, 8
	s_movk_i32 s5, 0xa00
	v_lshlrev_b32_e32 v184, 6, v4
	v_or_b32_e32 v4, 64, v4
	v_bitop3_b32 v195, v5, v6, 48 bitop3:0x6c
	v_lshl_add_u64 v[178:179], s[14:15], 0, v[170:171]
	v_lshl_add_u64 v[180:181], s[16:17], 0, v[2:3]
	s_addc_u32 s1, s1, 0
	v_mad_u32_u24 v1, v1, s5, 0
	v_lshrrev_b32_e32 v2, 3, v0
	s_movk_i32 s5, 0x50
	v_and_b32_e32 v170, 48, v169
	v_bfe_u32 v0, v0, 2, 4
	v_lshrrev_b32_e32 v5, 2, v4
	v_mov_b32_e32 v144, 0x38383838
	v_bfe_u32 v226, v169, 6, 1
	v_bfe_u32 v227, v169, 8, 1
	v_cmp_eq_u32_e32 vcc, v226, v227
	s_nop 1
	v_cndmask_b32_e32 v144, 0, v144, vcc
	v_lshl_add_u64 v[182:183], s[18:19], 0, v[6:7]
	v_and_b32_e32 v2, 4, v2
	v_mad_u32_u24 v3, v168, s5, v1
	s_add_u32 s12, s12, 0x4900000
	v_add_u32_e32 v1, v1, v170
	v_mul_u32_u24_e32 v0, 0x50, v0
	v_mul_u32_u24_e32 v5, 0x50, v5
	s_movk_i32 s18, 0xffc0
	v_lshlrev_b32_e32 v199, 6, v168
	s_mov_b32 s7, 0
	s_movk_i32 s3, 0x2000
	s_movk_i32 s33, 0x4000
	v_mov_b32_e32 v173, 0x74747474
	v_mov_b32_e32 v194, 0x7f7f7f7f
	v_mov_b32_e32 v145, v144
	v_mov_b32_e32 v146, v144
	v_mov_b32_e32 v147, v144
	v_mov_b32_e32 v148, v144
	v_mov_b32_e32 v149, v144
	v_mov_b32_e32 v150, v144
	v_mov_b32_e32 v151, v144
	s_addc_u32 s13, s13, 0
	v_mov_b32_e32 v185, v171
	v_lshlrev_b32_e32 v186, 6, v4
	v_mov_b32_e32 v187, v171
	s_mov_b64 s[30:31], -1
	s_mov_b64 s[14:15], 0x3000
	s_mov_b64 s[16:17], 0xc0
	s_mov_b32 s19, -1
	s_mov_b32 s5, 0xff61b1e6
	s_mov_b32 s36, 0x41000000
	s_mov_b64 s[20:21], 0x80
	s_mov_b64 s[22:23], 0x11000
	s_mov_b64 s[24:25], 0x400
	s_mov_b64 s[26:27], 0x440
	s_mov_b32 s37, 0x42800000
	v_add_u32_e32 v196, v3, v2
	v_add_u32_e32 v197, v1, v0
	v_add_u32_e32 v198, v1, v5
	v_add_u32_e32 v197, 0x10000, v197
	v_add_u32_e32 v198, 0x10000, v198
	v_mov_b32_e32 v0, v171
	v_mov_b32_e32 v1, v171
	v_mov_b32_e32 v2, v171
	v_mov_b32_e32 v3, v171
	v_mov_b32_e32 v4, v171
	v_mov_b32_e32 v5, v171
	v_mov_b32_e32 v6, v171
	v_mov_b32_e32 v8, v171
	v_mov_b32_e32 v9, v171
	v_mov_b32_e32 v10, v171
	v_mov_b32_e32 v11, v171
	v_mov_b32_e32 v12, v171
	v_mov_b32_e32 v13, v171
	v_mov_b32_e32 v14, v171
	v_mov_b32_e32 v15, v171
	s_mov_b32 s38, 0
	v_mov_b32_e32 v160, v171
	v_mov_b32_e32 v161, v171
	v_mov_b32_e32 v162, v171
	v_mov_b32_e32 v163, v171
	v_mov_b32_e32 v164, v171
	v_mov_b32_e32 v165, v171
	v_mov_b32_e32 v166, v171
	v_mov_b32_e32 v167, v171
	v_xor_b32_e32 v200, 16, v195
	v_add_u32_e32 v201, 0, v199
	v_add_u32_e32 v222, v199, v195
	v_add_u32_e32 v223, v199, v200
	v_readfirstlane_b32 s40, v169
	v_add_u32_e32 v224, 0x8000, v222
	v_add_u32_e32 v225, 0x8000, v223
	v_add_u32_e32 v228, 0x1000, v220
	v_add_u32_e32 v229, 64, v221
	s_add_u32 s60, s40, 0x0
	s_add_u32 s61, s40, 0x2000
	s_add_u32 s62, s40, 0x4000
	s_add_u32 s63, s40, 0x6000
	s_add_u32 s64, s40, 0x8000
	s_add_u32 s65, s40, 0xa000
	s_add_u32 s66, s40, 0xc000
	s_add_u32 s67, s40, 0xe000
	v_mov_b32_e32 v202, 0x12000
	s_branch .LBB3_3

.LBB3_2:
	v_exp_f32_e32 v81, v112
	v_exp_f32_e32 v82, v113
	v_exp_f32_e32 v85, v116
	v_exp_f32_e32 v86, v117
	v_exp_f32_e32 v89, v120
	v_exp_f32_e32 v90, v121
	v_exp_f32_e32 v93, v124
	v_exp_f32_e32 v94, v125
	v_exp_f32_e32 v64, v64
	v_exp_f32_e32 v65, v65
	v_exp_f32_e32 v68, v68
	v_exp_f32_e32 v69, v69
	v_exp_f32_e32 v72, v72
	v_exp_f32_e32 v73, v73
	v_exp_f32_e32 v76, v76
	v_exp_f32_e32 v77, v77
	v_exp_f32_e32 v83, v114
	v_exp_f32_e32 v84, v115
	v_exp_f32_e32 v87, v118
	v_exp_f32_e32 v88, v119
	v_exp_f32_e32 v91, v122
	v_exp_f32_e32 v92, v123
	v_exp_f32_e32 v95, v126
	v_exp_f32_e32 v96, v127
	v_exp_f32_e32 v66, v66
	v_exp_f32_e32 v67, v67
	v_exp_f32_e32 v70, v70
	v_exp_f32_e32 v71, v71
	v_exp_f32_e32 v74, v74
	v_exp_f32_e32 v75, v75
	v_exp_f32_e32 v78, v78
	v_exp_f32_e32 v79, v79
	v_cvt_pk_fp8_f32 v160, v81, v82
	v_cvt_pk_fp8_f32 v161, v85, v86
	v_cvt_pk_fp8_f32 v162, v89, v90
	v_cvt_pk_fp8_f32 v163, v93, v94
	v_cvt_pk_fp8_f32 v164, v64, v65
	v_cvt_pk_fp8_f32 v165, v68, v69
	v_cvt_pk_fp8_f32 v166, v72, v73
	v_cvt_pk_fp8_f32 v167, v76, v77
	v_cvt_pk_fp8_f32 v160, v83, v84 op_sel:[0,0,1]
	v_cvt_pk_fp8_f32 v161, v87, v88 op_sel:[0,0,1]
	v_cvt_pk_fp8_f32 v162, v91, v92 op_sel:[0,0,1]
	v_cvt_pk_fp8_f32 v163, v95, v96 op_sel:[0,0,1]
	v_cvt_pk_fp8_f32 v164, v66, v67 op_sel:[0,0,1]
	v_cvt_pk_fp8_f32 v165, v70, v71 op_sel:[0,0,1]
	v_cvt_pk_fp8_f32 v166, v74, v75 op_sel:[0,0,1]
	v_cvt_pk_fp8_f32 v167, v78, v79 op_sel:[0,0,1]
	s_lshl_b32 s6, s4, 7
	s_and_b32 s6, s6, 0xfffffc00
	v_mfma_scale_f32_16x16x128_f8f6f4 v[48:51], v[144:151], v[160:167], v[48:51], v194, v194 op_sel_hi:[0,0,0]
	s_nop 15
	s_nop 3
	s_lshl_b32 s4, s4, 6
	v_mul_f32_e32 v48, 0x41800000, v48
	s_waitcnt lgkmcnt(0)
	v_mfma_scale_f32_32x32x64_f8f6f4 v[32:47], v[128:135], v[160:167], v[32:47], v194, v194 op_sel_hi:[0,0,0]
	v_div_scale_f32 v49, s[30:31], v48, v48, s37
	v_rcp_f32_e32 v66, v49
	s_mov_b64 s[30:31], 0
	v_fma_f32 v50, -v49, v66, 1.0
	v_fmac_f32_e32 v66, v50, v66
	v_div_scale_f32 v50, vcc, s37, v48, s37
	v_mul_f32_e32 v51, v50, v66
	v_fma_f32 v52, -v49, v51, v50
	v_fmac_f32_e32 v51, v52, v66
	v_fma_f32 v49, -v49, v51, v50
	v_div_fmas_f32 v49, v49, v66, v51
	v_mfma_scale_f32_32x32x64_f8f6f4 v[16:31], v[136:143], v[160:167], v[16:31], v194, v194 op_sel_hi:[0,0,0]
	v_div_fixup_f32 v48, v49, v48, s37
	s_nop 6
	v_mul_f32_e32 v32, v48, v32
	v_mul_f32_e32 v33, v48, v33
	v_mov_b32_e32 v49, 0
	v_cvt_pk_fp8_f32 v49, v32, v33
	v_mul_f32_e32 v32, v48, v34
	v_mul_f32_e32 v33, v48, v35
	s_and_b64 vcc, exec, s[28:29]
	v_cvt_pk_fp8_f32 v49, v32, v33 op_sel:[0,0,1]
	v_mov_b32_e32 v32, 0
	v_mov_b32_e32 v33, 0
	s_nop 1
	v_mul_f32_e32 v16, v48, v16
	v_mul_f32_e32 v17, v48, v17
	v_cvt_pk_fp8_f32 v32, v16, v17
	v_mul_f32_e32 v16, v48, v36
	v_mul_f32_e32 v17, v48, v37
	v_cvt_pk_fp8_f32 v33, v16, v17
	v_mul_f32_e32 v18, v48, v18
	v_mul_f32_e32 v19, v48, v19
	v_mul_f32_e32 v16, v48, v38
	v_mul_f32_e32 v17, v48, v39
	v_cvt_pk_fp8_f32 v32, v18, v19 op_sel:[0,0,1]
	v_cvt_pk_fp8_f32 v33, v16, v17 op_sel:[0,0,1]
	v_mul_f32_e32 v16, v48, v20
	v_mul_f32_e32 v17, v48, v21
	v_mov_b32_e32 v18, 0
	v_cvt_pk_fp8_f32 v18, v16, v17
	v_mul_f32_e32 v17, v48, v22
	v_mul_f32_e32 v19, v48, v23
	v_mov_b32_e32 v22, 0
	v_cvt_pk_fp8_f32 v18, v17, v19 op_sel:[0,0,1]
	v_mul_f32_e32 v17, v48, v40
	v_mul_f32_e32 v19, v48, v41
	v_cvt_pk_fp8_f32 v22, v17, v19
	v_mul_f32_e32 v17, v48, v24
	v_mul_f32_e32 v19, v48, v25
	v_mov_b32_e32 v23, 0
	v_cvt_pk_fp8_f32 v23, v17, v19
	v_mul_f32_e32 v17, v48, v26
	v_mul_f32_e32 v19, v48, v27
	v_mov_b32_e32 v24, 0
	v_cvt_pk_fp8_f32 v23, v17, v19 op_sel:[0,0,1]
	v_mul_f32_e32 v17, v48, v44
	v_mul_f32_e32 v19, v48, v45
	v_cvt_pk_fp8_f32 v24, v17, v19
	v_mul_f32_e32 v17, v48, v28
	v_mul_f32_e32 v19, v48, v29
	v_mov_b32_e32 v25, 0
	v_cvt_pk_fp8_f32 v25, v17, v19
	v_mul_f32_e32 v20, v48, v42
	v_mul_f32_e32 v21, v48, v43
	v_cvt_pk_fp8_f32 v22, v20, v21 op_sel:[0,0,1]
	v_mul_f32_e32 v20, v48, v46
	v_mul_f32_e32 v21, v48, v47
	v_cvt_pk_fp8_f32 v24, v20, v21 op_sel:[0,0,1]
	v_mul_f32_e32 v17, v48, v30
	v_mul_f32_e32 v19, v48, v31
	v_add_u32_e32 v16, 0x10000, v196
	v_cvt_pk_fp8_f32 v25, v17, v19 op_sel:[0,0,1]
	ds_write2_b32 v16, v49, v33 offset1:2
	ds_write2_b32 v16, v32, v18 offset0:8 offset1:10
	ds_write2_b32 v16, v22, v24 offset0:4 offset1:6
	ds_write2_b32 v16, v23, v25 offset0:12 offset1:14
	v_add_u32_e32 v16, s6, v172
	v_ashrrev_i32_e32 v17, 31, v16
	s_waitcnt lgkmcnt(0)
	v_lshlrev_b64 v[16:17], 8, v[16:17]
	v_lshl_add_u64 v[20:21], s[12:13], 0, v[16:17]
	s_and_b32 s68, s4, 0x100
	s_lshl_b32 s68, s68, 14
	s_and_b32 s6, s4, 0xc0
	s_or_b32 s6, s6, s68
	ds_read_b128 v[16:19], v197
	v_lshl_add_u64 v[24:25], v[20:21], 0, s[6:7]
	ds_read_b128 v[20:23], v198
	v_lshl_add_u64 v[24:25], v[24:25], 0, v[170:171]
	v_lshl_add_u64 v[26:27], v[24:25], 0, v[184:185]
	s_waitcnt lgkmcnt(0)
	global_store_dwordx4 v[26:27], v[16:19], off
	s_mov_b32 s4, s34
	v_mov_b32_e32 v172, v80
	v_lshl_add_u64 v[16:17], v[24:25], 0, v[186:187]
	global_store_dwordx4 v[16:17], v[20:23], off
	s_waitcnt lgkmcnt(0)
	s_cbranch_vccnz .LBB3_18

	.amdhsa_kernel _Z13attn11_kernelILi4EEvPc
		.amdhsa_group_segment_fixed_size 16384
		.amdhsa_private_segment_fixed_size 0
		.amdhsa_kernarg_size 264
		.amdhsa_user_sgpr_count 2
		.amdhsa_user_sgpr_dispatch_ptr 0
		.amdhsa_user_sgpr_queue_ptr 0
		.amdhsa_user_sgpr_kernarg_segment_ptr 1
		.amdhsa_user_sgpr_dispatch_id 0
		.amdhsa_user_sgpr_kernarg_preload_length 0
		.amdhsa_user_sgpr_kernarg_preload_offset 0
		.amdhsa_user_sgpr_private_segment_size 0
		.amdhsa_uses_dynamic_stack 0
		.amdhsa_enable_private_segment 0
		.amdhsa_system_sgpr_workgroup_id_x 1
		.amdhsa_system_sgpr_workgroup_id_y 0
		.amdhsa_system_sgpr_workgroup_id_z 0
		.amdhsa_system_sgpr_workgroup_info 0
		.amdhsa_system_vgpr_workitem_id 0
		.amdhsa_next_free_vgpr 230
		.amdhsa_next_free_sgpr 70
		.amdhsa_accum_offset 232
		.amdhsa_reserve_vcc 1
		.amdhsa_float_round_mode_32 0
		.amdhsa_float_round_mode_16_64 0
		.amdhsa_float_denorm_mode_32 3
		.amdhsa_float_denorm_mode_16_64 3
		.amdhsa_dx10_clamp 1
		.amdhsa_ieee_mode 1
		.amdhsa_fp16_overflow 0
		.amdhsa_tg_split 0
		.amdhsa_exception_fp_ieee_invalid_op 0
		.amdhsa_exception_fp_denorm_src 0
		.amdhsa_exception_fp_ieee_div_zero 0
		.amdhsa_exception_fp_ieee_overflow 0
		.amdhsa_exception_fp_ieee_underflow 0
		.amdhsa_exception_fp_ieee_inexact 0
		.amdhsa_exception_int_div_zero 0
	.end_amdhsa_kernel

amdhsa.kernels:
  - .agpr_count:     0
    .args:
      - .actual_access:  read_only
        .address_space:  global
        .offset:         0
        .size:           8
        .value_kind:     global_buffer
      - .actual_access:  read_only
        .address_space:  global
        .offset:         8
        .size:           8
        .value_kind:     global_buffer
      - .actual_access:  read_only
        .address_space:  global
        .offset:         16
        .size:           8
        .value_kind:     global_buffer
      - .actual_access:  read_only
        .address_space:  global
        .offset:         24
        .size:           8
        .value_kind:     global_buffer
      - .actual_access:  read_only
        .address_space:  global
        .offset:         32
        .size:           8
        .value_kind:     global_buffer
      - .actual_access:  read_only
        .address_space:  global
        .offset:         40
        .size:           8
        .value_kind:     global_buffer
      - .actual_access:  read_only
        .address_space:  global
        .offset:         48
        .size:           8
        .value_kind:     global_buffer
      - .actual_access:  write_only
        .address_space:  global
        .offset:         56
        .size:           8
        .value_kind:     global_buffer
    .group_segment_fixed_size: 32
    .kernarg_segment_align: 8
    .kernarg_segment_size: 64
    .language:       OpenCL C
    .language_version:
      - 2
      - 0
    .max_flat_workgroup_size: 256
    .name:           _Z11prep_kernelPKfS0_S0_S0_S0_S0_S0_Pc
    .private_segment_fixed_size: 0
    .sgpr_count:     48
    .sgpr_spill_count: 0
    .symbol:         _Z11prep_kernelPKfS0_S0_S0_S0_S0_S0_Pc.kd
    .uniform_work_group_size: 1
    .uses_dynamic_stack: false
    .vgpr_count:     78
    .vgpr_spill_count: 0
    .wavefront_size: 64
  - .agpr_count:     0
    .args:
      - .address_space:  global
        .offset:         0
        .size:           8
        .value_kind:     global_buffer
      - .actual_access:  read_only
        .address_space:  global
        .offset:         8
        .size:           8
        .value_kind:     global_buffer
      - .actual_access:  read_only
        .address_space:  global
        .offset:         16
        .size:           8
        .value_kind:     global_buffer
    .group_segment_fixed_size: 0
    .kernarg_segment_align: 8
    .kernarg_segment_size: 24
    .language:       OpenCL C
    .language_version:
      - 2
      - 0
    .max_flat_workgroup_size: 512
    .name:           _Z13qkv256_kernelPcPKfS1_
    .private_segment_fixed_size: 0
    .sgpr_count:     35
    .sgpr_spill_count: 0
    .symbol:         _Z13qkv256_kernelPcPKfS1_.kd
    .uniform_work_group_size: 1
    .uses_dynamic_stack: false
    .vgpr_count:     214
    .vgpr_spill_count: 0
    .wavefront_size: 64
  - .agpr_count:     0
    .args:
      - .address_space:  global
        .offset:         0
        .size:           8
        .value_kind:     global_buffer
      - .actual_access:  read_only
        .address_space:  global
        .offset:         8
        .size:           8
        .value_kind:     global_buffer
      - .actual_access:  read_only
        .address_space:  global
        .offset:         16
        .size:           8
        .value_kind:     global_buffer
      - .actual_access:  write_only
        .address_space:  global
        .offset:         24
        .size:           8
        .value_kind:     global_buffer
    .group_segment_fixed_size: 0
    .kernarg_segment_align: 8
    .kernarg_segment_size: 32
    .language:       OpenCL C
    .language_version:
      - 2
      - 0
    .max_flat_workgroup_size: 256
    .name:           _Z11proj_kernelPKcPKfS2_Pf
    .private_segment_fixed_size: 0
    .sgpr_count:     34
    .sgpr_spill_count: 0
    .symbol:         _Z11proj_kernelPKcPKfS2_Pf.kd
    .uniform_work_group_size: 1
    .uses_dynamic_stack: false
    .vgpr_count:     194
    .vgpr_spill_count: 0
    .wavefront_size: 64
  - .agpr_count:     0
    .args:
      - .address_space:  global
        .offset:         0
        .size:           8
        .value_kind:     global_buffer
      - .offset:         8
        .size:           4
        .value_kind:     hidden_block_count_x
      - .offset:         12
        .size:           4
        .value_kind:     hidden_block_count_y
      - .offset:         16
        .size:           4
        .value_kind:     hidden_block_count_z
      - .offset:         20
        .size:           2
        .value_kind:     hidden_group_size_x
      - .offset:         22
        .size:           2
        .value_kind:     hidden_group_size_y
      - .offset:         24
        .size:           2
        .value_kind:     hidden_group_size_z
      - .offset:         26
        .size:           2
        .value_kind:     hidden_remainder_x
      - .offset:         28
        .size:           2
        .value_kind:     hidden_remainder_y
      - .offset:         30
        .size:           2
        .value_kind:     hidden_remainder_z
      - .offset:         48
        .size:           8
        .value_kind:     hidden_global_offset_x
      - .offset:         56
        .size:           8
        .value_kind:     hidden_global_offset_y
      - .offset:         64
        .size:           8
        .value_kind:     hidden_global_offset_z
      - .offset:         72
        .size:           2
        .value_kind:     hidden_grid_dims
      - .offset:         128
        .size:           4
        .value_kind:     hidden_dynamic_lds_size
    .group_segment_fixed_size: 16384
    .kernarg_segment_align: 8
    .kernarg_segment_size: 264
    .language:       OpenCL C
    .language_version:
      - 2
      - 0
    .max_flat_workgroup_size: 256
    .name:           _Z13attn11_kernelILi4EEvPc
    .private_segment_fixed_size: 0
    .sgpr_count:     76
    .sgpr_spill_count: 0
    .symbol:         _Z13attn11_kernelILi4EEvPc.kd
    .uniform_work_group_size: 1
    .uses_dynamic_stack: false
    .vgpr_count:     230
    .vgpr_spill_count: 0
    .wavefront_size: 64
